# stack6 = stack4 + GLA scan step's first LDS fragment reads issued right behind the staging barrier
# speedup vs baseline: 1.0027x; 1.0027x over previous
.LBB0_599:
	s_waitcnt vmcnt(12) lgkmcnt(14)
	v_mfma_f32_16x16x32_bf16 v[154:157], v[154:157], v[46:49], 0
	s_waitcnt vmcnt(11)
	v_mfma_f32_16x16x32_bf16 v[154:157], v[158:161], v[30:33], v[154:157]
	s_waitcnt lgkmcnt(13)
	v_mfma_f32_16x16x32_bf16 v[158:161], v[162:165], v[46:49], 0
	s_waitcnt lgkmcnt(12)
	v_mfma_f32_16x16x32_bf16 v[158:161], v[166:169], v[30:33], v[158:161]
	s_waitcnt lgkmcnt(11)
	v_mfma_f32_16x16x32_bf16 v[162:165], v[170:173], v[46:49], 0
	s_waitcnt lgkmcnt(9)
	v_mfma_f32_16x16x32_bf16 v[166:169], v[178:181], v[46:49], 0
	v_mfma_f32_16x16x32_bf16 v[162:165], v[174:177], v[30:33], v[162:165]
	s_waitcnt lgkmcnt(8)
	v_mfma_f32_16x16x32_bf16 v[166:169], v[182:185], v[30:33], v[166:169]
	ds_read_b128 v[170:173], v135 offset:128
	ds_read_b128 v[174:177], v135 offset:192
	ds_read_b128 v[178:181], v135 offset:8832
	ds_read_b128 v[182:185], v135 offset:8896
	ds_read_b128 v[220:223], v135 offset:17536
	ds_read_b128 v[224:227], v135 offset:17600
	ds_read_b128 v[228:231], v135 offset:26240
	ds_read_b128 v[232:235], v135 offset:26304
	v_cvt_pk_bf16_f32 v236, v106, v107
	v_cvt_pk_bf16_f32 v237, v108, v109
	v_cvt_pk_bf16_f32 v238, v102, v103
	v_cvt_pk_bf16_f32 v239, v104, v105
	s_waitcnt lgkmcnt(14)
	v_mfma_f32_16x16x32_bf16 v[154:157], v[186:189], v[236:239], v[154:157]
	v_cvt_pk_bf16_f32 v186, v98, v99
	v_cvt_pk_bf16_f32 v187, v100, v101
	v_cvt_pk_bf16_f32 v188, v94, v95
	s_waitcnt lgkmcnt(13)
	v_mfma_f32_16x16x32_bf16 v[158:161], v[194:197], v[236:239], v[158:161]
	v_cvt_pk_bf16_f32 v189, v96, v97
	s_waitcnt lgkmcnt(11)
	v_mfma_f32_16x16x32_bf16 v[162:165], v[202:205], v[236:239], v[162:165]
	s_waitcnt lgkmcnt(9)
	v_mfma_f32_16x16x32_bf16 v[166:169], v[210:213], v[236:239], v[166:169]
	v_mfma_f32_16x16x32_bf16 v[154:157], v[190:193], v[186:189], v[154:157]
	v_mfma_f32_16x16x32_bf16 v[158:161], v[198:201], v[186:189], v[158:161]
	v_mfma_f32_16x16x32_bf16 v[162:165], v[206:209], v[186:189], v[162:165]
	s_waitcnt lgkmcnt(8)
	v_mfma_f32_16x16x32_bf16 v[166:169], v[216:219], v[186:189], v[166:169]
	ds_read_b128 v[186:189], v135 offset:256
	ds_read_b128 v[190:193], v135 offset:320
	ds_read_b128 v[194:197], v135 offset:8960
	ds_read_b128 v[198:201], v135 offset:9024
	ds_read_b128 v[202:205], v135 offset:17664
	ds_read_b128 v[206:209], v135 offset:17728
	ds_read_b128 v[210:213], v135 offset:26368
	ds_read_b128 v[216:219], v135 offset:26432
	v_cvt_pk_bf16_f32 v236, v90, v91
	v_cvt_pk_bf16_f32 v237, v92, v93
	v_cvt_pk_bf16_f32 v238, v86, v87
	v_cvt_pk_bf16_f32 v239, v88, v89
	s_waitcnt lgkmcnt(14)
	v_mfma_f32_16x16x32_bf16 v[154:157], v[170:173], v[236:239], v[154:157]
	v_cvt_pk_bf16_f32 v170, v82, v83
	v_cvt_pk_bf16_f32 v171, v84, v85
	v_cvt_pk_bf16_f32 v172, v78, v79
	s_waitcnt lgkmcnt(13)
	v_mfma_f32_16x16x32_bf16 v[158:161], v[178:181], v[236:239], v[158:161]
	v_cvt_pk_bf16_f32 v173, v80, v81
	s_waitcnt lgkmcnt(11)
	v_mfma_f32_16x16x32_bf16 v[162:165], v[220:223], v[236:239], v[162:165]
	s_waitcnt lgkmcnt(9)
	v_mfma_f32_16x16x32_bf16 v[166:169], v[228:231], v[236:239], v[166:169]
	v_mfma_f32_16x16x32_bf16 v[154:157], v[174:177], v[170:173], v[154:157]
	v_mfma_f32_16x16x32_bf16 v[158:161], v[182:185], v[170:173], v[158:161]
	v_mfma_f32_16x16x32_bf16 v[162:165], v[224:227], v[170:173], v[162:165]
	s_waitcnt lgkmcnt(8)
	v_mfma_f32_16x16x32_bf16 v[166:169], v[232:235], v[170:173], v[166:169]
	ds_read_b128 v[170:173], v135 offset:384
	ds_read_b128 v[174:177], v135 offset:448
	ds_read_b128 v[178:181], v135 offset:9088
	ds_read_b128 v[182:185], v135 offset:9152
	ds_read_b128 v[220:223], v135 offset:17792
	ds_read_b128 v[224:227], v135 offset:17856
	ds_read_b128 v[228:231], v135 offset:26496
	ds_read_b128 v[232:235], v135 offset:26560
	v_cvt_pk_bf16_f32 v236, v74, v75
	v_cvt_pk_bf16_f32 v237, v76, v77
	v_cvt_pk_bf16_f32 v238, v70, v71
	v_cvt_pk_bf16_f32 v239, v72, v73
	s_waitcnt lgkmcnt(14)
	v_mfma_f32_16x16x32_bf16 v[154:157], v[186:189], v[236:239], v[154:157]
	v_cvt_pk_bf16_f32 v186, v66, v67
	v_cvt_pk_bf16_f32 v187, v68, v69
	v_cvt_pk_bf16_f32 v188, v62, v63
	s_waitcnt lgkmcnt(13)
	v_mfma_f32_16x16x32_bf16 v[158:161], v[194:197], v[236:239], v[158:161]
	v_cvt_pk_bf16_f32 v189, v64, v65
	s_waitcnt lgkmcnt(11)
	v_mfma_f32_16x16x32_bf16 v[162:165], v[202:205], v[236:239], v[162:165]
	s_waitcnt lgkmcnt(9)
	v_mfma_f32_16x16x32_bf16 v[166:169], v[210:213], v[236:239], v[166:169]
	v_mfma_f32_16x16x32_bf16 v[154:157], v[190:193], v[186:189], v[154:157]
	v_mfma_f32_16x16x32_bf16 v[158:161], v[198:201], v[186:189], v[158:161]
	v_mfma_f32_16x16x32_bf16 v[162:165], v[206:209], v[186:189], v[162:165]
	s_waitcnt lgkmcnt(8)
	v_mfma_f32_16x16x32_bf16 v[166:169], v[216:219], v[186:189], v[166:169]
	ds_read_b128 v[186:189], v134 offset:34816
	ds_read_b128 v[190:193], v134 offset:34880
	ds_read_b128 v[194:197], v137
	ds_read_b128 v[198:201], v137 offset:16
	ds_read_b128 v[202:205], v134 offset:37376
	ds_read_b128 v[206:209], v134 offset:37440
	ds_read_b128 v[210:213], v134 offset:39936
	ds_read_b128 v[216:219], v134 offset:40000
	ds_read_b128 v[236:239], v134 offset:42496
	ds_read_b128 v[240:243], v134 offset:42560
	ds_read_b128 v[244:247], v137 offset:128
	ds_read_b128 v[248:251], v137 offset:144
	v_cvt_pk_bf16_f32 v126, v58, v59
	v_cvt_pk_bf16_f32 v127, v60, v61
	v_cvt_pk_bf16_f32 v128, v54, v55
	v_cvt_pk_bf16_f32 v129, v56, v57
	s_waitcnt lgkmcnt(14)
	v_mfma_f32_16x16x32_bf16 v[154:157], v[170:173], v[126:129], v[154:157]
	v_mfma_f32_16x16x32_bf16 v[158:161], v[178:181], v[126:129], v[158:161]
	v_mfma_f32_16x16x32_bf16 v[162:165], v[220:223], v[126:129], v[162:165]
	s_waitcnt lgkmcnt(13)
	v_mfma_f32_16x16x32_bf16 v[126:129], v[228:231], v[126:129], v[166:169]
	v_cvt_pk_bf16_f32 v166, v50, v51
	v_cvt_pk_bf16_f32 v167, v52, v53
	v_cvt_pk_bf16_f32 v168, v110, v111
	v_cvt_pk_bf16_f32 v169, v112, v113
	s_nop 0
	v_mfma_f32_16x16x32_bf16 v[154:157], v[174:177], v[166:169], v[154:157]
	v_mfma_f32_16x16x32_bf16 v[158:161], v[182:185], v[166:169], v[158:161]
	v_mfma_f32_16x16x32_bf16 v[162:165], v[224:227], v[166:169], v[162:165]
	s_waitcnt lgkmcnt(12)
	v_mfma_f32_16x16x32_bf16 v[126:129], v[232:235], v[166:169], v[126:129]
	s_bitcmp1_b32 s9, 0
	s_cselect_b32 s9, 0x4400, 0
	v_add_u32_e32 v166, s9, v143
	v_cvt_pk_bf16_f32 v154, v154, v155
	v_cvt_pk_bf16_f32 v155, v156, v157
	s_nop 0
	ds_write_b16 v166, v154
	ds_write_b16_d16_hi v166, v154 offset:272
	ds_write_b16 v166, v155 offset:544
	ds_write_b16_d16_hi v166, v155 offset:816
	v_cvt_pk_bf16_f32 v154, v158, v159
	v_cvt_pk_bf16_f32 v155, v160, v161
	ds_write_b16 v166, v154 offset:4352
	ds_write_b16_d16_hi v166, v154 offset:4624
	ds_write_b16 v166, v155 offset:4896
	ds_write_b16_d16_hi v166, v155 offset:5168
	v_cvt_pk_bf16_f32 v154, v162, v163
	v_cvt_pk_bf16_f32 v155, v164, v165
	ds_write_b16 v166, v154 offset:8704
	ds_write_b16_d16_hi v166, v154 offset:8976
	ds_write_b16 v166, v155 offset:9248
	ds_write_b16_d16_hi v166, v155 offset:9520
	v_cvt_pk_bf16_f32 v126, v126, v127
	v_cvt_pk_bf16_f32 v127, v128, v129
	ds_write_b16 v166, v126 offset:13056
	ds_write_b16_d16_hi v166, v126 offset:13328
	ds_write_b16 v166, v127 offset:13600
	ds_write_b16_d16_hi v166, v127 offset:13872
	ds_read_b128 v[126:129], v134 offset:45056
	ds_read_b128 v[154:157], v134 offset:45120
	ds_read_b128 v[158:161], v137 offset:256
	ds_read_b128 v[162:165], v137 offset:272
	ds_read_b128 v[166:169], v134 offset:47616
	ds_read_b128 v[170:173], v134 offset:47680
	ds_read_b128 v[174:177], v134 offset:50176
	ds_read_b128 v[178:181], v134 offset:50240
	ds_read_b128 v[182:185], v134 offset:52736
	ds_read_b128 v[220:223], v134 offset:52800
	ds_read_b128 v[224:227], v137 offset:384
	ds_read_b128 v[228:231], v137 offset:400
	s_waitcnt lgkmcnt(14)
	v_pk_mul_f32 v[108:109], v[108:109], v[196:197]
	v_pk_mul_f32 v[106:107], v[106:107], v[194:195]
	v_pk_mul_f32 v[104:105], v[104:105], v[200:201]
	v_pk_mul_f32 v[102:103], v[102:103], v[198:199]
	v_pk_mul_f32 v[100:101], v[100:101], v[246:247]
	v_pk_mul_f32 v[98:99], v[98:99], v[244:245]
	v_pk_mul_f32 v[96:97], v[96:97], v[250:251]
	v_pk_mul_f32 v[94:95], v[94:95], v[248:249]
	v_mfma_f32_16x16x32_bf16 v[106:109], v[186:189], v[46:49], v[106:109]
	v_mfma_f32_16x16x32_bf16 v[102:105], v[202:205], v[46:49], v[102:105]
	v_mfma_f32_16x16x32_bf16 v[98:101], v[210:213], v[46:49], v[98:101]
	v_mfma_f32_16x16x32_bf16 v[94:97], v[236:239], v[46:49], v[94:97]
	v_mfma_f32_16x16x32_bf16 v[106:109], v[190:193], v[30:33], v[106:109]
	v_mfma_f32_16x16x32_bf16 v[102:105], v[206:209], v[30:33], v[102:105]
	v_mfma_f32_16x16x32_bf16 v[98:101], v[216:219], v[30:33], v[98:101]
	v_mfma_f32_16x16x32_bf16 v[94:97], v[240:243], v[30:33], v[94:97]
	ds_read_b128 v[186:189], v134 offset:55296
	ds_read_b128 v[190:193], v134 offset:55360
	ds_read_b128 v[194:197], v137 offset:512
	ds_read_b128 v[198:201], v137 offset:528
	ds_read_b128 v[202:205], v134 offset:57856
	ds_read_b128 v[206:209], v134 offset:57920
	ds_read_b128 v[210:213], v134 offset:60416
	ds_read_b128 v[216:219], v134 offset:60480
	ds_read_b128 v[232:235], v134 offset:62976
	ds_read_b128 v[236:239], v134 offset:63040
	ds_read_b128 v[240:243], v137 offset:640
	ds_read_b128 v[244:247], v137 offset:656
	s_waitcnt lgkmcnt(14)
	v_pk_mul_f32 v[92:93], v[92:93], v[160:161]
	v_pk_mul_f32 v[90:91], v[90:91], v[158:159]
	v_pk_mul_f32 v[88:89], v[88:89], v[164:165]
	v_pk_mul_f32 v[86:87], v[86:87], v[162:163]
	s_waitcnt lgkmcnt(13)
	v_pk_mul_f32 v[84:85], v[84:85], v[226:227]
	v_pk_mul_f32 v[82:83], v[82:83], v[224:225]
	s_waitcnt lgkmcnt(12)
	v_pk_mul_f32 v[80:81], v[80:81], v[230:231]
	v_pk_mul_f32 v[78:79], v[78:79], v[228:229]
	v_mfma_f32_16x16x32_bf16 v[90:93], v[126:129], v[46:49], v[90:93]
	v_mfma_f32_16x16x32_bf16 v[86:89], v[166:169], v[46:49], v[86:89]
	v_mfma_f32_16x16x32_bf16 v[82:85], v[174:177], v[46:49], v[82:85]
	v_mfma_f32_16x16x32_bf16 v[78:81], v[182:185], v[46:49], v[78:81]
	v_mfma_f32_16x16x32_bf16 v[90:93], v[154:157], v[30:33], v[90:93]
	v_mfma_f32_16x16x32_bf16 v[86:89], v[170:173], v[30:33], v[86:89]
	v_mfma_f32_16x16x32_bf16 v[82:85], v[178:181], v[30:33], v[82:85]
	v_mfma_f32_16x16x32_bf16 v[78:81], v[220:223], v[30:33], v[78:81]
	ds_read_b128 v[126:129], v136 offset:30720
	ds_read_b128 v[154:157], v136 offset:30784
	ds_read_b128 v[158:161], v137 offset:768
	ds_read_b128 v[162:165], v137 offset:784
	ds_read_b128 v[166:169], v136 offset:33280
	ds_read_b128 v[170:173], v136 offset:33344
	ds_read_b128 v[174:177], v136 offset:35840
	ds_read_b128 v[178:181], v136 offset:35904
	ds_read_b128 v[182:185], v136 offset:38400
	ds_read_b128 v[220:223], v136 offset:38464
	ds_read_b128 v[224:227], v137 offset:896
	ds_read_b128 v[228:231], v137 offset:912
	s_waitcnt lgkmcnt(14)
	v_pk_mul_f32 v[76:77], v[76:77], v[196:197]
	v_pk_mul_f32 v[74:75], v[74:75], v[194:195]
	v_pk_mul_f32 v[72:73], v[72:73], v[200:201]
	v_pk_mul_f32 v[70:71], v[70:71], v[198:199]
	s_waitcnt lgkmcnt(13)
	v_pk_mul_f32 v[68:69], v[68:69], v[242:243]
	v_pk_mul_f32 v[66:67], v[66:67], v[240:241]
	s_waitcnt lgkmcnt(12)
	v_pk_mul_f32 v[64:65], v[64:65], v[246:247]
	v_pk_mul_f32 v[62:63], v[62:63], v[244:245]
	v_mfma_f32_16x16x32_bf16 v[74:77], v[186:189], v[46:49], v[74:77]
	v_mfma_f32_16x16x32_bf16 v[70:73], v[202:205], v[46:49], v[70:73]
	v_mfma_f32_16x16x32_bf16 v[66:69], v[210:213], v[46:49], v[66:69]
	v_mfma_f32_16x16x32_bf16 v[62:65], v[232:235], v[46:49], v[62:65]
	v_mfma_f32_16x16x32_bf16 v[74:77], v[190:193], v[30:33], v[74:77]
	v_mfma_f32_16x16x32_bf16 v[70:73], v[206:209], v[30:33], v[70:73]
	v_mfma_f32_16x16x32_bf16 v[66:69], v[216:219], v[30:33], v[66:69]
	v_mfma_f32_16x16x32_bf16 v[62:65], v[236:239], v[30:33], v[62:65]
	s_waitcnt lgkmcnt(9)
	v_pk_mul_f32 v[60:61], v[60:61], v[160:161]
	v_pk_mul_f32 v[58:59], v[58:59], v[158:159]
	s_waitcnt lgkmcnt(8)
	v_pk_mul_f32 v[56:57], v[56:57], v[164:165]
	v_pk_mul_f32 v[54:55], v[54:55], v[162:163]
	s_waitcnt lgkmcnt(1)
	v_pk_mul_f32 v[52:53], v[52:53], v[226:227]
	v_pk_mul_f32 v[50:51], v[50:51], v[224:225]
	s_waitcnt lgkmcnt(0)
	v_pk_mul_f32 v[112:113], v[112:113], v[230:231]
	v_pk_mul_f32 v[110:111], v[110:111], v[228:229]
	v_mfma_f32_16x16x32_bf16 v[58:61], v[126:129], v[46:49], v[58:61]
	s_add_i32 s15, s15, -1
	s_cmp_eq_u32 s15, 4
	s_mov_b32 s9, s22
	v_mfma_f32_16x16x32_bf16 v[54:57], v[166:169], v[46:49], v[54:57]
	v_mfma_f32_16x16x32_bf16 v[50:53], v[174:177], v[46:49], v[50:53]
	v_mfma_f32_16x16x32_bf16 v[46:49], v[182:185], v[46:49], v[110:113]
	v_mfma_f32_16x16x32_bf16 v[58:61], v[154:157], v[30:33], v[58:61]
	v_mfma_f32_16x16x32_bf16 v[54:57], v[170:173], v[30:33], v[54:57]
	v_mfma_f32_16x16x32_bf16 v[50:53], v[178:181], v[30:33], v[50:53]
	v_mfma_f32_16x16x32_bf16 v[110:113], v[220:223], v[30:33], v[46:49]
	s_waitcnt vmcnt(0)
	v_mov_b64_e32 v[30:31], v[118:119]
	v_mov_b64_e32 v[32:33], v[120:121]
	s_nop 0
	v_mov_b64_e32 v[46:47], v[114:115]
	v_mov_b64_e32 v[48:49], v[116:117]
	s_cbranch_scc1 .LBB0_619
.LBB0_600:
	s_waitcnt lgkmcnt(0)
	s_barrier
	s_waitcnt vmcnt(10)
	ds_write_b128 v150, v[22:25]
	s_waitcnt vmcnt(9)
	ds_write_b128 v145, v[6:9] offset:34816
	s_waitcnt vmcnt(8)
	ds_write_b128 v151, v[10:13]
	s_waitcnt vmcnt(7)
	ds_write_b128 v146, v[14:17] offset:34816
	s_waitcnt vmcnt(6)
	ds_write_b128 v152, v[18:21]
	s_waitcnt vmcnt(5)
	ds_write_b128 v148, v[26:29] offset:34816
	s_waitcnt vmcnt(4)
	ds_write_b128 v153, v[34:37]
	s_waitcnt vmcnt(3)
	ds_write_b128 v149, v[38:41] offset:34816
	s_waitcnt vmcnt(2)
	ds_write_b128 v139, v[42:45]
	s_mov_b64 s[10:11], exec
	v_readlane_b32 s12, v255, 2
	v_readlane_b32 s13, v255, 3
	s_and_b64 s[12:13], s[10:11], s[12:13]
	s_mov_b64 exec, s[12:13]
	v_add_u32_e32 v114, 0, v122
	v_add_u32_e32 v114, 0x15000, v114
	ds_write_b128 v114, v[2:5]
	s_or_b64 exec, exec, s[10:11]
	s_waitcnt lgkmcnt(0)
	s_barrier
	ds_read_b128 v[154:157], v133
	ds_read_b128 v[158:161], v133 offset:64
	ds_read_b128 v[162:165], v133 offset:2560
	ds_read_b128 v[166:169], v133 offset:2624
	ds_read_b128 v[170:173], v133 offset:5120
	ds_read_b128 v[174:177], v133 offset:5184
	ds_read_b128 v[178:181], v133 offset:7680
	ds_read_b128 v[182:185], v133 offset:7744
	ds_read_b128 v[186:189], v135
	ds_read_b128 v[190:193], v135 offset:64
	ds_read_b128 v[194:197], v135 offset:8704
	ds_read_b128 v[198:201], v135 offset:8768
	ds_read_b128 v[202:205], v135 offset:17408
	ds_read_b128 v[206:209], v135 offset:17472
	ds_read_b128 v[210:213], v135 offset:26112
	ds_read_b128 v[216:219], v135 offset:26176
	s_cmp_eq_u32 s9, 0
	s_cbranch_scc1 .LBB0_610
	s_mov_b64 s[10:11], -1
	s_and_b64 vcc, exec, s[6:7]
	s_cbranch_vccz .LBB0_607
	s_cmp_gt_u32 s9, 4
	s_mov_b32 s12, s15
	s_cbranch_scc1 .LBB0_606
	s_sub_i32 s12, 4, s9
